# DSA steady loop trims on top of the table mask: no m0 save/restore around LDS-DMAs, any-lane slow test from the existing lane mask, x+0 removed
# speedup vs baseline: 1.2752x; 1.0005x over previous
.LBB0_1077:
	v_lshl_add_u64 v[14:15], v[184:185], 0, s[54:55]
	s_mov_b32 s38, 0xeb20000
	v_add_co_u32_e32 v2, vcc, s38, v14
	s_mov_b32 s38, 0xeb28000
	s_nop 0
	v_addc_co_u32_e32 v3, vcc, 0, v15, vcc
	v_add_co_u32_e32 v4, vcc, s38, v14
	v_add_u32_e32 v12, s29, v239
	s_nop 0
	v_addc_co_u32_e32 v5, vcc, 0, v15, vcc
	global_load_dword v0, v[2:3], off
	global_load_dword v190, v[4:5], off
	global_load_dword v191, v[182:183], off offset:-4
	v_lshrrev_b32_e32 v2, v238, v211
	v_lshrrev_b32_e32 v3, v238, v213
	v_bfe_u32 v4, v2, 0, 4
	v_lshl_add_u32 v4, v4, 4, s100
	ds_read_b128 v[80:83], v4
	v_bfe_u32 v4, v2, 8, 4
	v_lshl_add_u32 v4, v4, 4, s100
	ds_read_b128 v[84:87], v4
	v_bfe_u32 v4, v2, 16, 4
	v_lshl_add_u32 v4, v4, 4, s100
	ds_read_b128 v[88:91], v4
	v_bfe_u32 v4, v2, 24, 4
	v_lshl_add_u32 v4, v4, 4, s100
	ds_read_b128 v[92:95], v4
	v_bfe_u32 v4, v3, 0, 4
	v_lshl_add_u32 v4, v4, 4, s100
	ds_read_b128 v[96:99], v4
	v_bfe_u32 v4, v3, 8, 4
	v_lshl_add_u32 v4, v4, 4, s100
	ds_read_b128 v[100:103], v4
	v_bfe_u32 v4, v3, 16, 4
	v_lshl_add_u32 v4, v4, 4, s100
	ds_read_b128 v[104:107], v4
	v_bfe_u32 v4, v3, 24, 4
	v_lshl_add_u32 v4, v4, 4, s100
	ds_read_b128 v[108:111], v4
	ds_read_b64_tr_b16 v[176:177], v12 offset:24576
	ds_read_b64_tr_b16 v[178:179], v12 offset:25088
	s_waitcnt lgkmcnt(6)
	v_mfma_f32_32x32x16_bf16 v[80:95], v[172:175], v[124:127], v[80:95]
	v_add_f32_e32 v2, v64, v65
	v_add_f32_e32 v2, v66, v2
	v_add_f32_e32 v2, v67, v2
	v_add_f32_e32 v2, v68, v2
	v_add_f32_e32 v2, v69, v2
	v_cvt_pk_bf16_f32 v140, v64, v65
	v_cvt_pk_bf16_f32 v141, v66, v67
	ds_read_b64_tr_b16 v[172:173], v12 offset:28672
	ds_read_b64_tr_b16 v[174:175], v12 offset:29184
	s_waitcnt lgkmcnt(4)
	v_mfma_f32_32x32x16_bf16 v[96:111], v[164:167], v[124:127], v[96:111]
	v_add_f32_e32 v2, v70, v2
	v_add_f32_e32 v2, v71, v2
	v_add_f32_e32 v2, v72, v2
	v_add_f32_e32 v2, v73, v2
	v_cvt_pk_bf16_f32 v142, v68, v69
	v_cvt_pk_bf16_f32 v143, v70, v71
	ds_read_b64_tr_b16 v[164:165], v12 offset:25600
	ds_read_b64_tr_b16 v[166:167], v12 offset:26112
	s_waitcnt lgkmcnt(11)
	v_mfma_f32_32x32x16_bf16 v[80:95], v[168:171], v[120:123], v[80:95]
	v_add_f32_e32 v2, v74, v2
	v_add_f32_e32 v2, v75, v2
	v_add_f32_e32 v2, v76, v2
	v_add_f32_e32 v2, v77, v2
	v_cvt_pk_bf16_f32 v136, v72, v73
	v_cvt_pk_bf16_f32 v137, v74, v75
	ds_read_b64_tr_b16 v[168:169], v12 offset:29696
	ds_read_b64_tr_b16 v[170:171], v12 offset:30208
	s_waitcnt lgkmcnt(12)
	v_mfma_f32_32x32x16_bf16 v[96:111], v[160:163], v[120:123], v[96:111]
	v_add_f32_e32 v2, v78, v2
	v_add_f32_e32 v2, v79, v2
	v_add_f32_e32 v2, v48, v2
	v_add_f32_e32 v2, v49, v2
	v_cvt_pk_bf16_f32 v138, v76, v77
	v_cvt_pk_bf16_f32 v139, v78, v79
	ds_read_b64_tr_b16 v[160:161], v12 offset:26624
	ds_read_b64_tr_b16 v[162:163], v12 offset:27136
	s_waitcnt lgkmcnt(13)
	v_mfma_f32_32x32x16_bf16 v[80:95], v[156:159], v[116:119], v[80:95]
	v_add_f32_e32 v2, v50, v2
	v_add_f32_e32 v2, v51, v2
	v_add_f32_e32 v2, v52, v2
	v_add_f32_e32 v6, v53, v2
	v_cvt_pk_bf16_f32 v132, v48, v49
	v_cvt_pk_bf16_f32 v133, v50, v51
	ds_read_b64_tr_b16 v[2:3], v12 offset:30720
	ds_read_b64_tr_b16 v[4:5], v12 offset:31232
	s_waitcnt lgkmcnt(14)
	v_mfma_f32_32x32x16_bf16 v[96:111], v[152:155], v[116:119], v[96:111]
	v_add_f32_e32 v6, v54, v6
	v_add_f32_e32 v6, v55, v6
	v_add_f32_e32 v6, v56, v6
	v_add_f32_e32 v10, v57, v6
	v_cvt_pk_bf16_f32 v134, v52, v53
	v_cvt_pk_bf16_f32 v135, v54, v55
	ds_read_b64_tr_b16 v[6:7], v12 offset:27648
	ds_read_b64_tr_b16 v[8:9], v12 offset:28160
	s_waitcnt lgkmcnt(14)
	v_mfma_f32_32x32x16_bf16 v[80:95], v[148:151], v[112:115], v[80:95]
	v_add_f32_e32 v10, v58, v10
	v_add_f32_e32 v10, v59, v10
	v_add_f32_e32 v10, v60, v10
	v_add_f32_e32 v48, v61, v10
	v_cvt_pk_bf16_f32 v128, v56, v57
	v_cvt_pk_bf16_f32 v129, v58, v59
	ds_read_b64_tr_b16 v[10:11], v12 offset:31744
	ds_read_b64_tr_b16 v[12:13], v12 offset:32256
	v_mfma_f32_32x32x16_bf16 v[96:111], v[144:147], v[112:115], v[96:111]
	v_add_f32_e32 v48, v62, v48
	v_add_f32_e32 v48, v63, v48
	v_cvt_pk_bf16_f32 v130, v60, v61
	v_cvt_pk_bf16_f32 v131, v62, v63
	v_lshl_add_u64 v[186:187], v[216:217], 0, s[54:55]
	v_lshl_add_u64 v[50:51], v[186:187], 0, s[20:21]
	s_add_i32 s29, s59, s63
	s_mov_b32 m0, s29
	s_nop 0
	global_load_lds_dwordx4 v[50:51], off
	v_lshl_add_u64 v[188:189], v[218:219], 0, s[54:55]
	v_lshl_add_u64 v[50:51], v[188:189], 0, s[24:25]
	s_add_i32 s29, s57, s62
	s_mov_b32 m0, s29
	s_nop 0
	global_load_lds_dwordx4 v[50:51], off
	s_waitcnt vmcnt(7)
	v_mul_f32_e32 v49, v201, v209
	v_cmp_nge_f32_e32 vcc, s73, v49
	v_cmp_neq_f32_e64 s[38:39], 0, v207
	s_or_b64 vcc, vcc, s[38:39]
	s_cmp_lg_u64 vcc, 0
	s_cselect_b64 s[38:39], -1, 0
	s_cbranch_vccz .LBB0_1079
	v_sub_f32_e32 v95, v95, v207
	v_sub_f32_e32 v94, v94, v207
	v_sub_f32_e32 v93, v93, v207
	v_sub_f32_e32 v92, v92, v207
	v_sub_f32_e32 v91, v91, v207
	v_sub_f32_e32 v90, v90, v207
	v_sub_f32_e32 v89, v89, v207
	v_sub_f32_e32 v88, v88, v207
	v_sub_f32_e32 v87, v87, v207
	v_sub_f32_e32 v86, v86, v207
	v_sub_f32_e32 v85, v85, v207
	v_sub_f32_e32 v84, v84, v207
	v_sub_f32_e32 v83, v83, v207
	v_sub_f32_e32 v82, v82, v207
	v_sub_f32_e32 v81, v81, v207
	v_sub_f32_e32 v80, v80, v207
	v_sub_f32_e32 v111, v111, v207
	v_sub_f32_e32 v110, v110, v207
	v_sub_f32_e32 v109, v109, v207
	v_sub_f32_e32 v108, v108, v207
	v_sub_f32_e32 v107, v107, v207
	v_sub_f32_e32 v106, v106, v207
	v_sub_f32_e32 v105, v105, v207
	v_sub_f32_e32 v104, v104, v207
	v_sub_f32_e32 v103, v103, v207
	v_sub_f32_e32 v102, v102, v207
	v_sub_f32_e32 v101, v101, v207
	v_sub_f32_e32 v100, v100, v207
	v_sub_f32_e32 v99, v99, v207
	v_sub_f32_e32 v98, v98, v207
	v_sub_f32_e32 v97, v97, v207
	v_sub_f32_e32 v96, v96, v207

.LBB0_1082:
	s_add_i32 s29, s57, 0x2000
	s_cmpk_lg_i32 s57, 0x4000
	s_cselect_b32 s65, s29, 0
	v_add_co_u32_e32 v2, vcc, 0xeb30000, v14
	v_add_u32_e32 v12, s59, v239
	s_nop 0
	v_addc_co_u32_e32 v3, vcc, 0, v15, vcc
	global_load_dword v192, v[2:3], off
	v_add_co_u32_e32 v2, vcc, 0xeb38000, v14
	s_nop 1
	v_addc_co_u32_e32 v3, vcc, 0, v15, vcc
	global_load_dword v14, v[2:3], off
	global_load_dword v209, v[182:183], off
	v_lshrrev_b32_e32 v2, v238, v0
	v_lshrrev_b32_e32 v3, v238, v190
	v_bfe_u32 v4, v2, 0, 4
	v_lshl_add_u32 v4, v4, 4, s100
	ds_read_b128 v[80:83], v4
	v_bfe_u32 v4, v2, 8, 4
	v_lshl_add_u32 v4, v4, 4, s100
	ds_read_b128 v[84:87], v4
	v_bfe_u32 v4, v2, 16, 4
	v_lshl_add_u32 v4, v4, 4, s100
	ds_read_b128 v[88:91], v4
	v_bfe_u32 v4, v2, 24, 4
	v_lshl_add_u32 v4, v4, 4, s100
	ds_read_b128 v[92:95], v4
	v_bfe_u32 v4, v3, 0, 4
	v_lshl_add_u32 v4, v4, 4, s100
	ds_read_b128 v[96:99], v4
	v_bfe_u32 v4, v3, 8, 4
	v_lshl_add_u32 v4, v4, 4, s100
	ds_read_b128 v[100:103], v4
	v_bfe_u32 v4, v3, 16, 4
	v_lshl_add_u32 v4, v4, 4, s100
	ds_read_b128 v[104:107], v4
	v_bfe_u32 v4, v3, 24, 4
	v_lshl_add_u32 v4, v4, 4, s100
	ds_read_b128 v[108:111], v4
	ds_read_b64_tr_b16 v[156:157], v12 offset:24576
	ds_read_b64_tr_b16 v[158:159], v12 offset:25088
	s_waitcnt lgkmcnt(6)
	v_mfma_f32_32x32x16_bf16 v[80:95], v[140:143], v[124:127], v[80:95]
	v_add_f32_e32 v2, v64, v65
	v_add_f32_e32 v2, v66, v2
	v_add_f32_e32 v2, v67, v2
	v_add_f32_e32 v2, v68, v2
	v_add_f32_e32 v2, v69, v2
	v_cvt_pk_bf16_f32 v140, v64, v65
	v_cvt_pk_bf16_f32 v141, v66, v67
	ds_read_b64_tr_b16 v[152:153], v12 offset:28672
	ds_read_b64_tr_b16 v[154:155], v12 offset:29184
	s_waitcnt lgkmcnt(4)
	v_mfma_f32_32x32x16_bf16 v[96:111], v[136:139], v[124:127], v[96:111]
	v_add_f32_e32 v2, v70, v2
	v_add_f32_e32 v2, v71, v2
	v_add_f32_e32 v2, v72, v2
	v_add_f32_e32 v2, v73, v2
	v_cvt_pk_bf16_f32 v142, v68, v69
	v_cvt_pk_bf16_f32 v143, v70, v71
	ds_read_b64_tr_b16 v[144:145], v12 offset:25600
	ds_read_b64_tr_b16 v[146:147], v12 offset:26112
	s_waitcnt lgkmcnt(11)
	v_mfma_f32_32x32x16_bf16 v[80:95], v[148:151], v[120:123], v[80:95]
	v_add_f32_e32 v2, v74, v2
	v_add_f32_e32 v2, v75, v2
	v_add_f32_e32 v2, v76, v2
	v_add_f32_e32 v2, v77, v2
	v_cvt_pk_bf16_f32 v136, v72, v73
	v_cvt_pk_bf16_f32 v137, v74, v75
	ds_read_b64_tr_b16 v[148:149], v12 offset:29696
	ds_read_b64_tr_b16 v[150:151], v12 offset:30208
	s_waitcnt lgkmcnt(12)
	v_mfma_f32_32x32x16_bf16 v[96:111], v[176:179], v[120:123], v[96:111]
	v_add_f32_e32 v2, v78, v2
	v_add_f32_e32 v2, v79, v2
	v_add_f32_e32 v2, v48, v2
	v_add_f32_e32 v2, v49, v2
	v_cvt_pk_bf16_f32 v138, v76, v77
	v_cvt_pk_bf16_f32 v139, v78, v79
	ds_read_b64_tr_b16 v[176:177], v12 offset:26624
	ds_read_b64_tr_b16 v[178:179], v12 offset:27136
	s_waitcnt lgkmcnt(13)
	v_mfma_f32_32x32x16_bf16 v[80:95], v[172:175], v[116:119], v[80:95]
	v_add_f32_e32 v2, v50, v2
	v_add_f32_e32 v2, v51, v2
	v_add_f32_e32 v2, v52, v2
	v_add_f32_e32 v6, v53, v2
	v_cvt_pk_bf16_f32 v132, v48, v49
	v_cvt_pk_bf16_f32 v133, v50, v51
	ds_read_b64_tr_b16 v[2:3], v12 offset:30720
	ds_read_b64_tr_b16 v[4:5], v12 offset:31232
	s_waitcnt lgkmcnt(14)
	v_mfma_f32_32x32x16_bf16 v[96:111], v[164:167], v[116:119], v[96:111]
	v_add_f32_e32 v6, v54, v6
	v_add_f32_e32 v6, v55, v6
	v_add_f32_e32 v6, v56, v6
	v_add_f32_e32 v10, v57, v6
	v_cvt_pk_bf16_f32 v134, v52, v53
	v_cvt_pk_bf16_f32 v135, v54, v55
	ds_read_b64_tr_b16 v[6:7], v12 offset:27648
	ds_read_b64_tr_b16 v[8:9], v12 offset:28160
	s_waitcnt lgkmcnt(14)
	v_mfma_f32_32x32x16_bf16 v[80:95], v[168:171], v[112:115], v[80:95]
	v_add_f32_e32 v10, v58, v10
	v_add_f32_e32 v10, v59, v10
	v_add_f32_e32 v10, v60, v10
	v_add_f32_e32 v15, v61, v10
	v_cvt_pk_bf16_f32 v128, v56, v57
	v_cvt_pk_bf16_f32 v129, v58, v59
	ds_read_b64_tr_b16 v[10:11], v12 offset:31744
	ds_read_b64_tr_b16 v[12:13], v12 offset:32256
	v_mfma_f32_32x32x16_bf16 v[96:111], v[160:163], v[112:115], v[96:111]
	v_add_f32_e32 v15, v62, v15
	v_add_f32_e32 v15, v63, v15
	v_cvt_pk_bf16_f32 v130, v60, v61
	v_cvt_pk_bf16_f32 v131, v62, v63
	v_lshl_add_u64 v[48:49], v[186:187], 0, s[22:23]
	s_add_i32 s29, s57, s63
	s_mov_b32 m0, s29
	s_nop 0
	global_load_lds_dwordx4 v[48:49], off
	v_lshl_add_u64 v[48:49], v[188:189], 0, s[70:71]
	s_add_i32 s29, s65, s62
	s_mov_b32 m0, s29
	s_nop 0
	global_load_lds_dwordx4 v[48:49], off
	s_waitcnt vmcnt(7)
	v_mul_f32_e32 v48, v201, v191
	v_cmp_nge_f32_e32 vcc, s73, v48
	v_cmp_neq_f32_e64 s[38:39], 0, v207
	s_or_b64 vcc, vcc, s[38:39]
	s_cmp_lg_u64 vcc, 0
	s_cselect_b64 s[38:39], -1, 0
	s_cbranch_vccz .LBB0_1084
	v_sub_f32_e32 v95, v95, v207
	v_sub_f32_e32 v94, v94, v207
	v_sub_f32_e32 v93, v93, v207
	v_sub_f32_e32 v92, v92, v207
	v_sub_f32_e32 v91, v91, v207
	v_sub_f32_e32 v90, v90, v207
	v_sub_f32_e32 v89, v89, v207
	v_sub_f32_e32 v88, v88, v207
	v_sub_f32_e32 v87, v87, v207
	v_sub_f32_e32 v86, v86, v207
	v_sub_f32_e32 v85, v85, v207
	v_sub_f32_e32 v84, v84, v207
	v_sub_f32_e32 v83, v83, v207
	v_sub_f32_e32 v82, v82, v207
	v_sub_f32_e32 v81, v81, v207
	v_sub_f32_e32 v80, v80, v207
	v_sub_f32_e32 v111, v111, v207
	v_sub_f32_e32 v110, v110, v207
	v_sub_f32_e32 v109, v109, v207
	v_sub_f32_e32 v108, v108, v207
	v_sub_f32_e32 v107, v107, v207
	v_sub_f32_e32 v106, v106, v207
	v_sub_f32_e32 v105, v105, v207
	v_sub_f32_e32 v104, v104, v207
	v_sub_f32_e32 v103, v103, v207
	v_sub_f32_e32 v102, v102, v207
	v_sub_f32_e32 v101, v101, v207
	v_sub_f32_e32 v100, v100, v207
	v_sub_f32_e32 v99, v99, v207
	v_sub_f32_e32 v98, v98, v207
	v_sub_f32_e32 v97, v97, v207
	v_sub_f32_e32 v96, v96, v207
